# CSR sort window = (col*168)>>20 (25 windows of ~6240 rows) instead of 4700-row windows
# baseline (speedup 1.0000x reference)
.LBB3_46:
	s_and_b64 vcc, exec, s[0:1]
	s_cbranch_vccz .LBB3_141
	s_ashr_i32 s37, s36, 31
	s_lshl_b64 s[0:1], s[36:37], 3
	s_add_u32 s0, s2, s0
	s_addc_u32 s1, s3, s1
	s_add_i32 s8, s44, 31
	s_lshr_b32 s8, s8, 5
	s_add_i32 s8, s8, -1
	s_lshl_b32 s9, s42, 2
	s_sub_i32 s8, s8, s9
	s_bfe_u32 s8, s8, 0x1000a
	s_mul_i32 s8, s8, 31
	v_mov_b32_e32 v50, 0
	v_mov_b32_e32 v51, 0
	v_mov_b32_e32 v52, 0
	v_mov_b32_e32 v53, 0
	v_lshlrev_b32_e32 v1, 4, v0
	ds_write_b128 v1, v[50:53]
	v_mov_b32_e32 v63, 1
	v_add_u32_e32 v54, 0, v0
	v_lshl_add_u32 v54, v54, 1, 0
	v_cmp_gt_i32_e32 vcc, s33, v54
	v_lshlrev_b32_e32 v54, 3, v54
	s_and_saveexec_b64 s[4:5], vcc
	global_load_dwordx4 v[2:5], v54, s[0:1]
	s_or_b64 exec, exec, s[4:5]
	v_add_u32_e32 v54, 1024, v0
	v_lshl_add_u32 v54, v54, 1, 0
	v_cmp_gt_i32_e32 vcc, s33, v54
	v_lshlrev_b32_e32 v54, 3, v54
	s_and_saveexec_b64 s[4:5], vcc
	global_load_dwordx4 v[6:9], v54, s[0:1]
	s_or_b64 exec, exec, s[4:5]
	v_add_u32_e32 v54, 2048, v0
	v_lshl_add_u32 v54, v54, 1, 0
	v_cmp_gt_i32_e32 vcc, s33, v54
	v_lshlrev_b32_e32 v54, 3, v54
	s_and_saveexec_b64 s[4:5], vcc
	global_load_dwordx4 v[10:13], v54, s[0:1]
	s_or_b64 exec, exec, s[4:5]
	v_add_u32_e32 v54, 3072, v0
	v_lshl_add_u32 v54, v54, 1, 0
	v_cmp_gt_i32_e32 vcc, s33, v54
	v_lshlrev_b32_e32 v54, 3, v54
	s_and_saveexec_b64 s[4:5], vcc
	global_load_dwordx4 v[14:17], v54, s[0:1]
	s_or_b64 exec, exec, s[4:5]
	v_add_u32_e32 v54, 4096, v0
	v_lshl_add_u32 v54, v54, 1, 0
	v_cmp_gt_i32_e32 vcc, s33, v54
	v_lshlrev_b32_e32 v54, 3, v54
	s_and_saveexec_b64 s[4:5], vcc
	global_load_dwordx4 v[18:21], v54, s[0:1]
	s_or_b64 exec, exec, s[4:5]
	v_add_u32_e32 v54, 5120, v0
	v_lshl_add_u32 v54, v54, 1, 0
	v_cmp_gt_i32_e32 vcc, s33, v54
	v_lshlrev_b32_e32 v54, 3, v54
	s_and_saveexec_b64 s[4:5], vcc
	global_load_dwordx4 v[22:25], v54, s[0:1]
	s_or_b64 exec, exec, s[4:5]
	v_add_u32_e32 v54, 6144, v0
	v_lshl_add_u32 v54, v54, 1, 0
	v_cmp_gt_i32_e32 vcc, s33, v54
	v_lshlrev_b32_e32 v54, 3, v54
	s_and_saveexec_b64 s[4:5], vcc
	global_load_dwordx4 v[26:29], v54, s[0:1]
	s_or_b64 exec, exec, s[4:5]
	v_add_u32_e32 v54, 7168, v0
	v_lshl_add_u32 v54, v54, 1, 0
	v_cmp_gt_i32_e32 vcc, s33, v54
	v_lshlrev_b32_e32 v54, 3, v54
	s_and_saveexec_b64 s[4:5], vcc
	global_load_dwordx4 v[30:33], v54, s[0:1]
	s_or_b64 exec, exec, s[4:5]
	s_waitcnt lgkmcnt(0)
	s_barrier
	s_waitcnt vmcnt(7)
	v_lshrrev_b32_e32 v54, 25, v2
	v_mul_u32_u24_e32 v55, 0xa8, v2
	v_lshrrev_b32_e32 v55, 20, v55
	v_min_u32_e32 v55, 31, v55
	v_xor_b32_e32 v55, s8, v55
	v_lshl_or_b32 v54, v54, 5, v55
	v_lshlrev_b32_e32 v56, 2, v54
	v_add_u32_e32 v54, 0, v0
	v_lshl_add_u32 v54, v54, 1, 0
	v_cmp_gt_i32_e32 vcc, s33, v54
	s_and_saveexec_b64 s[4:5], vcc
	ds_add_rtn_u32 v34, v56, v63
	s_or_b64 exec, exec, s[4:5]
	s_waitcnt vmcnt(7)
	v_lshrrev_b32_e32 v54, 25, v4
	v_mul_u32_u24_e32 v55, 0xa8, v4
	v_lshrrev_b32_e32 v55, 20, v55
	v_min_u32_e32 v55, 31, v55
	v_xor_b32_e32 v55, s8, v55
	v_lshl_or_b32 v54, v54, 5, v55
	v_lshlrev_b32_e32 v56, 2, v54
	v_add_u32_e32 v54, 0, v0
	v_lshl_add_u32 v54, v54, 1, 1
	v_cmp_gt_i32_e32 vcc, s33, v54
	s_and_saveexec_b64 s[4:5], vcc
	ds_add_rtn_u32 v35, v56, v63
	s_or_b64 exec, exec, s[4:5]
	s_waitcnt vmcnt(6)
	v_lshrrev_b32_e32 v54, 25, v6
	v_mul_u32_u24_e32 v55, 0xa8, v6
	v_lshrrev_b32_e32 v55, 20, v55
	v_min_u32_e32 v55, 31, v55
	v_xor_b32_e32 v55, s8, v55
	v_lshl_or_b32 v54, v54, 5, v55
	v_lshlrev_b32_e32 v56, 2, v54
	v_add_u32_e32 v54, 1024, v0
	v_lshl_add_u32 v54, v54, 1, 0
	v_cmp_gt_i32_e32 vcc, s33, v54
	s_and_saveexec_b64 s[4:5], vcc
	ds_add_rtn_u32 v36, v56, v63
	s_or_b64 exec, exec, s[4:5]
	s_waitcnt vmcnt(6)
	v_lshrrev_b32_e32 v54, 25, v8
	v_mul_u32_u24_e32 v55, 0xa8, v8
	v_lshrrev_b32_e32 v55, 20, v55
	v_min_u32_e32 v55, 31, v55
	v_xor_b32_e32 v55, s8, v55
	v_lshl_or_b32 v54, v54, 5, v55
	v_lshlrev_b32_e32 v56, 2, v54
	v_add_u32_e32 v54, 1024, v0
	v_lshl_add_u32 v54, v54, 1, 1
	v_cmp_gt_i32_e32 vcc, s33, v54
	s_and_saveexec_b64 s[4:5], vcc
	ds_add_rtn_u32 v37, v56, v63
	s_or_b64 exec, exec, s[4:5]
	s_waitcnt vmcnt(5)
	v_lshrrev_b32_e32 v54, 25, v10
	v_mul_u32_u24_e32 v55, 0xa8, v10
	v_lshrrev_b32_e32 v55, 20, v55
	v_min_u32_e32 v55, 31, v55
	v_xor_b32_e32 v55, s8, v55
	v_lshl_or_b32 v54, v54, 5, v55
	v_lshlrev_b32_e32 v56, 2, v54
	v_add_u32_e32 v54, 2048, v0
	v_lshl_add_u32 v54, v54, 1, 0
	v_cmp_gt_i32_e32 vcc, s33, v54
	s_and_saveexec_b64 s[4:5], vcc
	ds_add_rtn_u32 v38, v56, v63
	s_or_b64 exec, exec, s[4:5]
	s_waitcnt vmcnt(5)
	v_lshrrev_b32_e32 v54, 25, v12
	v_mul_u32_u24_e32 v55, 0xa8, v12
	v_lshrrev_b32_e32 v55, 20, v55
	v_min_u32_e32 v55, 31, v55
	v_xor_b32_e32 v55, s8, v55
	v_lshl_or_b32 v54, v54, 5, v55
	v_lshlrev_b32_e32 v56, 2, v54
	v_add_u32_e32 v54, 2048, v0
	v_lshl_add_u32 v54, v54, 1, 1
	v_cmp_gt_i32_e32 vcc, s33, v54
	s_and_saveexec_b64 s[4:5], vcc
	ds_add_rtn_u32 v39, v56, v63
	s_or_b64 exec, exec, s[4:5]
	s_waitcnt vmcnt(4)
	v_lshrrev_b32_e32 v54, 25, v14
	v_mul_u32_u24_e32 v55, 0xa8, v14
	v_lshrrev_b32_e32 v55, 20, v55
	v_min_u32_e32 v55, 31, v55
	v_xor_b32_e32 v55, s8, v55
	v_lshl_or_b32 v54, v54, 5, v55
	v_lshlrev_b32_e32 v56, 2, v54
	v_add_u32_e32 v54, 3072, v0
	v_lshl_add_u32 v54, v54, 1, 0
	v_cmp_gt_i32_e32 vcc, s33, v54
	s_and_saveexec_b64 s[4:5], vcc
	ds_add_rtn_u32 v40, v56, v63
	s_or_b64 exec, exec, s[4:5]
	s_waitcnt vmcnt(4)
	v_lshrrev_b32_e32 v54, 25, v16
	v_mul_u32_u24_e32 v55, 0xa8, v16
	v_lshrrev_b32_e32 v55, 20, v55
	v_min_u32_e32 v55, 31, v55
	v_xor_b32_e32 v55, s8, v55
	v_lshl_or_b32 v54, v54, 5, v55
	v_lshlrev_b32_e32 v56, 2, v54
	v_add_u32_e32 v54, 3072, v0
	v_lshl_add_u32 v54, v54, 1, 1
	v_cmp_gt_i32_e32 vcc, s33, v54
	s_and_saveexec_b64 s[4:5], vcc
	ds_add_rtn_u32 v41, v56, v63
	s_or_b64 exec, exec, s[4:5]
	s_waitcnt vmcnt(3)
	v_lshrrev_b32_e32 v54, 25, v18
	v_mul_u32_u24_e32 v55, 0xa8, v18
	v_lshrrev_b32_e32 v55, 20, v55
	v_min_u32_e32 v55, 31, v55
	v_xor_b32_e32 v55, s8, v55
	v_lshl_or_b32 v54, v54, 5, v55
	v_lshlrev_b32_e32 v56, 2, v54
	v_add_u32_e32 v54, 4096, v0
	v_lshl_add_u32 v54, v54, 1, 0
	v_cmp_gt_i32_e32 vcc, s33, v54
	s_and_saveexec_b64 s[4:5], vcc
	ds_add_rtn_u32 v42, v56, v63
	s_or_b64 exec, exec, s[4:5]
	s_waitcnt vmcnt(3)
	v_lshrrev_b32_e32 v54, 25, v20
	v_mul_u32_u24_e32 v55, 0xa8, v20
	v_lshrrev_b32_e32 v55, 20, v55
	v_min_u32_e32 v55, 31, v55
	v_xor_b32_e32 v55, s8, v55
	v_lshl_or_b32 v54, v54, 5, v55
	v_lshlrev_b32_e32 v56, 2, v54
	v_add_u32_e32 v54, 4096, v0
	v_lshl_add_u32 v54, v54, 1, 1
	v_cmp_gt_i32_e32 vcc, s33, v54
	s_and_saveexec_b64 s[4:5], vcc
	ds_add_rtn_u32 v43, v56, v63
	s_or_b64 exec, exec, s[4:5]
	s_waitcnt vmcnt(2)
	v_lshrrev_b32_e32 v54, 25, v22
	v_mul_u32_u24_e32 v55, 0xa8, v22
	v_lshrrev_b32_e32 v55, 20, v55
	v_min_u32_e32 v55, 31, v55
	v_xor_b32_e32 v55, s8, v55
	v_lshl_or_b32 v54, v54, 5, v55
	v_lshlrev_b32_e32 v56, 2, v54
	v_add_u32_e32 v54, 5120, v0
	v_lshl_add_u32 v54, v54, 1, 0
	v_cmp_gt_i32_e32 vcc, s33, v54
	s_and_saveexec_b64 s[4:5], vcc
	ds_add_rtn_u32 v44, v56, v63
	s_or_b64 exec, exec, s[4:5]
	s_waitcnt vmcnt(2)
	v_lshrrev_b32_e32 v54, 25, v24
	v_mul_u32_u24_e32 v55, 0xa8, v24
	v_lshrrev_b32_e32 v55, 20, v55
	v_min_u32_e32 v55, 31, v55
	v_xor_b32_e32 v55, s8, v55
	v_lshl_or_b32 v54, v54, 5, v55
	v_lshlrev_b32_e32 v56, 2, v54
	v_add_u32_e32 v54, 5120, v0
	v_lshl_add_u32 v54, v54, 1, 1
	v_cmp_gt_i32_e32 vcc, s33, v54
	s_and_saveexec_b64 s[4:5], vcc
	ds_add_rtn_u32 v45, v56, v63
	s_or_b64 exec, exec, s[4:5]
	s_waitcnt vmcnt(1)
	v_lshrrev_b32_e32 v54, 25, v26
	v_mul_u32_u24_e32 v55, 0xa8, v26
	v_lshrrev_b32_e32 v55, 20, v55
	v_min_u32_e32 v55, 31, v55
	v_xor_b32_e32 v55, s8, v55
	v_lshl_or_b32 v54, v54, 5, v55
	v_lshlrev_b32_e32 v56, 2, v54
	v_add_u32_e32 v54, 6144, v0
	v_lshl_add_u32 v54, v54, 1, 0
	v_cmp_gt_i32_e32 vcc, s33, v54
	s_and_saveexec_b64 s[4:5], vcc
	ds_add_rtn_u32 v46, v56, v63
	s_or_b64 exec, exec, s[4:5]
	s_waitcnt vmcnt(1)
	v_lshrrev_b32_e32 v54, 25, v28
	v_mul_u32_u24_e32 v55, 0xa8, v28
	v_lshrrev_b32_e32 v55, 20, v55
	v_min_u32_e32 v55, 31, v55
	v_xor_b32_e32 v55, s8, v55
	v_lshl_or_b32 v54, v54, 5, v55
	v_lshlrev_b32_e32 v56, 2, v54
	v_add_u32_e32 v54, 6144, v0
	v_lshl_add_u32 v54, v54, 1, 1
	v_cmp_gt_i32_e32 vcc, s33, v54
	s_and_saveexec_b64 s[4:5], vcc
	ds_add_rtn_u32 v47, v56, v63
	s_or_b64 exec, exec, s[4:5]
	s_waitcnt vmcnt(0)
	v_lshrrev_b32_e32 v54, 25, v30
	v_mul_u32_u24_e32 v55, 0xa8, v30
	v_lshrrev_b32_e32 v55, 20, v55
	v_min_u32_e32 v55, 31, v55
	v_xor_b32_e32 v55, s8, v55
	v_lshl_or_b32 v54, v54, 5, v55
	v_lshlrev_b32_e32 v56, 2, v54
	v_add_u32_e32 v54, 7168, v0
	v_lshl_add_u32 v54, v54, 1, 0
	v_cmp_gt_i32_e32 vcc, s33, v54
	s_and_saveexec_b64 s[4:5], vcc
	ds_add_rtn_u32 v48, v56, v63
	s_or_b64 exec, exec, s[4:5]
	s_waitcnt vmcnt(0)
	v_lshrrev_b32_e32 v54, 25, v32
	v_mul_u32_u24_e32 v55, 0xa8, v32
	v_lshrrev_b32_e32 v55, 20, v55
	v_min_u32_e32 v55, 31, v55
	v_xor_b32_e32 v55, s8, v55
	v_lshl_or_b32 v54, v54, 5, v55
	v_lshlrev_b32_e32 v56, 2, v54
	v_add_u32_e32 v54, 7168, v0
	v_lshl_add_u32 v54, v54, 1, 1
	v_cmp_gt_i32_e32 vcc, s33, v54
	s_and_saveexec_b64 s[4:5], vcc
	ds_add_rtn_u32 v49, v56, v63
	s_or_b64 exec, exec, s[4:5]
	s_waitcnt lgkmcnt(0)
	s_barrier
	ds_read_b128 v[50:53], v1
	v_mbcnt_lo_u32_b32 v54, -1, 0
	v_mbcnt_hi_u32_b32 v54, -1, v54
	v_lshrrev_b32_e32 v55, 6, v0
	s_waitcnt lgkmcnt(0)
	v_add_u32_e32 v56, v50, v51
	v_add_u32_e32 v57, v56, v52
	v_add_u32_e32 v58, v57, v53
	v_mov_b32_e32 v59, v58
	v_subrev_u32_e32 v61, 1, v54
	v_lshlrev_b32_e32 v61, 2, v61
	ds_bpermute_b32 v60, v61, v59
	v_cmp_le_u32_e32 vcc, 1, v54
	s_waitcnt lgkmcnt(0)
	v_cndmask_b32_e32 v60, 0, v60, vcc
	v_add_u32_e32 v59, v59, v60
	v_subrev_u32_e32 v61, 2, v54
	v_lshlrev_b32_e32 v61, 2, v61
	ds_bpermute_b32 v60, v61, v59
	v_cmp_le_u32_e32 vcc, 2, v54
	s_waitcnt lgkmcnt(0)
	v_cndmask_b32_e32 v60, 0, v60, vcc
	v_add_u32_e32 v59, v59, v60
	v_subrev_u32_e32 v61, 4, v54
	v_lshlrev_b32_e32 v61, 2, v61
	ds_bpermute_b32 v60, v61, v59
	v_cmp_le_u32_e32 vcc, 4, v54
	s_waitcnt lgkmcnt(0)
	v_cndmask_b32_e32 v60, 0, v60, vcc
	v_add_u32_e32 v59, v59, v60
	v_subrev_u32_e32 v61, 8, v54
	v_lshlrev_b32_e32 v61, 2, v61
	ds_bpermute_b32 v60, v61, v59
	v_cmp_le_u32_e32 vcc, 8, v54
	s_waitcnt lgkmcnt(0)
	v_cndmask_b32_e32 v60, 0, v60, vcc
	v_add_u32_e32 v59, v59, v60
	v_subrev_u32_e32 v61, 16, v54
	v_lshlrev_b32_e32 v61, 2, v61
	ds_bpermute_b32 v60, v61, v59
	v_cmp_le_u32_e32 vcc, 16, v54
	s_waitcnt lgkmcnt(0)
	v_cndmask_b32_e32 v60, 0, v60, vcc
	v_add_u32_e32 v59, v59, v60
	v_subrev_u32_e32 v61, 32, v54
	v_lshlrev_b32_e32 v61, 2, v61
	ds_bpermute_b32 v60, v61, v59
	v_cmp_le_u32_e32 vcc, 32, v54
	s_waitcnt lgkmcnt(0)
	v_cndmask_b32_e32 v60, 0, v60, vcc
	v_add_u32_e32 v59, v59, v60
	v_lshlrev_b32_e32 v61, 2, v55
	v_cmp_eq_u32_e32 vcc, 63, v54
	s_and_saveexec_b64 s[4:5], vcc
	ds_write_b32 v61, v59 offset:16384
	s_or_b64 exec, exec, s[4:5]
	s_waitcnt lgkmcnt(0)
	s_barrier
	v_mov_b32_e32 v54, 0
	v_mov_b32_e32 v61, 0
	ds_read_b128 v[60:63], v61 offset:16384
	s_waitcnt lgkmcnt(0)
	v_cmp_lt_u32_e32 vcc, 0, v55
	s_nop 1
	v_cndmask_b32_e32 v60, 0, v60, vcc
	v_add_u32_e32 v54, v54, v60
	v_cmp_lt_u32_e32 vcc, 1, v55
	s_nop 1
	v_cndmask_b32_e32 v61, 0, v61, vcc
	v_add_u32_e32 v54, v54, v61
	v_cmp_lt_u32_e32 vcc, 2, v55
	s_nop 1
	v_cndmask_b32_e32 v62, 0, v62, vcc
	v_add_u32_e32 v54, v54, v62
	v_cmp_lt_u32_e32 vcc, 3, v55
	s_nop 1
	v_cndmask_b32_e32 v63, 0, v63, vcc
	v_add_u32_e32 v54, v54, v63
	v_mov_b32_e32 v61, 0
	ds_read_b128 v[60:63], v61 offset:16400
	s_waitcnt lgkmcnt(0)
	v_cmp_lt_u32_e32 vcc, 4, v55
	s_nop 1
	v_cndmask_b32_e32 v60, 0, v60, vcc
	v_add_u32_e32 v54, v54, v60
	v_cmp_lt_u32_e32 vcc, 5, v55
	s_nop 1
	v_cndmask_b32_e32 v61, 0, v61, vcc
	v_add_u32_e32 v54, v54, v61
	v_cmp_lt_u32_e32 vcc, 6, v55
	s_nop 1
	v_cndmask_b32_e32 v62, 0, v62, vcc
	v_add_u32_e32 v54, v54, v62
	v_cmp_lt_u32_e32 vcc, 7, v55
	s_nop 1
	v_cndmask_b32_e32 v63, 0, v63, vcc
	v_add_u32_e32 v54, v54, v63
	v_mov_b32_e32 v61, 0
	ds_read_b128 v[60:63], v61 offset:16416
	s_waitcnt lgkmcnt(0)
	v_cmp_lt_u32_e32 vcc, 8, v55
	s_nop 1
	v_cndmask_b32_e32 v60, 0, v60, vcc
	v_add_u32_e32 v54, v54, v60
	v_cmp_lt_u32_e32 vcc, 9, v55
	s_nop 1
	v_cndmask_b32_e32 v61, 0, v61, vcc
	v_add_u32_e32 v54, v54, v61
	v_cmp_lt_u32_e32 vcc, 10, v55
	s_nop 1
	v_cndmask_b32_e32 v62, 0, v62, vcc
	v_add_u32_e32 v54, v54, v62
	v_cmp_lt_u32_e32 vcc, 11, v55
	s_nop 1
	v_cndmask_b32_e32 v63, 0, v63, vcc
	v_add_u32_e32 v54, v54, v63
	v_mov_b32_e32 v61, 0
	ds_read_b128 v[60:63], v61 offset:16432
	s_waitcnt lgkmcnt(0)
	v_cmp_lt_u32_e32 vcc, 12, v55
	s_nop 1
	v_cndmask_b32_e32 v60, 0, v60, vcc
	v_add_u32_e32 v54, v54, v60
	v_cmp_lt_u32_e32 vcc, 13, v55
	s_nop 1
	v_cndmask_b32_e32 v61, 0, v61, vcc
	v_add_u32_e32 v54, v54, v61
	v_cmp_lt_u32_e32 vcc, 14, v55
	s_nop 1
	v_cndmask_b32_e32 v62, 0, v62, vcc
	v_add_u32_e32 v54, v54, v62
	v_mov_b32_e32 v62, v54
	v_sub_u32_e32 v59, v59, v58
	v_add_u32_e32 v59, v59, v62
	v_add_u32_e32 v60, v59, v50
	v_add_u32_e32 v61, v59, v56
	v_add_u32_e32 v62, v59, v57
	v_mov_b32_e32 v50, v59
	v_mov_b32_e32 v51, v60
	v_mov_b32_e32 v52, v61
	v_mov_b32_e32 v53, v62
	ds_write_b128 v1, v[50:53]
	v_and_b32_e32 v56, 7, v0
	v_lshrrev_b32_e32 v57, 3, v0
	v_lshl_add_u32 v57, s42, 7, v57
	v_cmp_eq_u32_e32 vcc, 0, v56
	v_cmp_gt_i32_e64 s[4:5], s44, v57
	s_and_b64 s[4:5], vcc, s[4:5]
	v_add_u32_e32 v58, s36, v59
	v_lshlrev_b32_e32 v56, 2, v57
	s_and_saveexec_b64 s[10:11], s[4:5]
	global_store_dword v56, v58, s[38:39]
	s_add_i32 s7, s44, -1
	v_cmp_eq_u32_e32 vcc, s7, v57
	s_and_b64 exec, exec, vcc
	v_mov_b32_e32 v58, s45
	global_store_dword v56, v58, s[38:39] offset:4
	s_mov_b64 exec, s[10:11]
	s_waitcnt lgkmcnt(0)
	s_barrier
	v_lshrrev_b32_e32 v54, 25, v2
	v_mul_u32_u24_e32 v55, 0xa8, v2
	v_lshrrev_b32_e32 v55, 20, v55
	v_min_u32_e32 v55, 31, v55
	v_xor_b32_e32 v55, s8, v55
	v_lshl_or_b32 v54, v54, 5, v55
	v_lshlrev_b32_e32 v56, 2, v54
	ds_read_b32 v56, v56
	v_lshrrev_b32_e32 v54, 25, v4
	v_mul_u32_u24_e32 v55, 0xa8, v4
	v_lshrrev_b32_e32 v55, 20, v55
	v_min_u32_e32 v55, 31, v55
	v_xor_b32_e32 v55, s8, v55
	v_lshl_or_b32 v54, v54, 5, v55
	v_lshlrev_b32_e32 v57, 2, v54
	ds_read_b32 v57, v57
	v_lshrrev_b32_e32 v54, 25, v6
	v_mul_u32_u24_e32 v55, 0xa8, v6
	v_lshrrev_b32_e32 v55, 20, v55
	v_min_u32_e32 v55, 31, v55
	v_xor_b32_e32 v55, s8, v55
	v_lshl_or_b32 v54, v54, 5, v55
	v_lshlrev_b32_e32 v58, 2, v54
	ds_read_b32 v58, v58
	v_lshrrev_b32_e32 v54, 25, v8
	v_mul_u32_u24_e32 v55, 0xa8, v8
	v_lshrrev_b32_e32 v55, 20, v55
	v_min_u32_e32 v55, 31, v55
	v_xor_b32_e32 v55, s8, v55
	v_lshl_or_b32 v54, v54, 5, v55
	v_lshlrev_b32_e32 v59, 2, v54
	ds_read_b32 v59, v59
	s_waitcnt lgkmcnt(0)
	v_add_u32_e32 v34, v34, v56
	v_and_b32_e32 v2, 0x1ffffff, v2
	v_add_u32_e32 v35, v35, v57
	v_and_b32_e32 v4, 0x1ffffff, v4
	v_add_u32_e32 v36, v36, v58
	v_and_b32_e32 v6, 0x1ffffff, v6
	v_add_u32_e32 v37, v37, v59
	v_and_b32_e32 v8, 0x1ffffff, v8
	v_lshrrev_b32_e32 v54, 25, v10
	v_mul_u32_u24_e32 v55, 0xa8, v10
	v_lshrrev_b32_e32 v55, 20, v55
	v_min_u32_e32 v55, 31, v55
	v_xor_b32_e32 v55, s8, v55
	v_lshl_or_b32 v54, v54, 5, v55
	v_lshlrev_b32_e32 v56, 2, v54
	ds_read_b32 v56, v56
	v_lshrrev_b32_e32 v54, 25, v12
	v_mul_u32_u24_e32 v55, 0xa8, v12
	v_lshrrev_b32_e32 v55, 20, v55
	v_min_u32_e32 v55, 31, v55
	v_xor_b32_e32 v55, s8, v55
	v_lshl_or_b32 v54, v54, 5, v55
	v_lshlrev_b32_e32 v57, 2, v54
	ds_read_b32 v57, v57
	v_lshrrev_b32_e32 v54, 25, v14
	v_mul_u32_u24_e32 v55, 0xa8, v14
	v_lshrrev_b32_e32 v55, 20, v55
	v_min_u32_e32 v55, 31, v55
	v_xor_b32_e32 v55, s8, v55
	v_lshl_or_b32 v54, v54, 5, v55
	v_lshlrev_b32_e32 v58, 2, v54
	ds_read_b32 v58, v58
	v_lshrrev_b32_e32 v54, 25, v16
	v_mul_u32_u24_e32 v55, 0xa8, v16
	v_lshrrev_b32_e32 v55, 20, v55
	v_min_u32_e32 v55, 31, v55
	v_xor_b32_e32 v55, s8, v55
	v_lshl_or_b32 v54, v54, 5, v55
	v_lshlrev_b32_e32 v59, 2, v54
	ds_read_b32 v59, v59
	s_waitcnt lgkmcnt(0)
	v_add_u32_e32 v38, v38, v56
	v_and_b32_e32 v10, 0x1ffffff, v10
	v_add_u32_e32 v39, v39, v57
	v_and_b32_e32 v12, 0x1ffffff, v12
	v_add_u32_e32 v40, v40, v58
	v_and_b32_e32 v14, 0x1ffffff, v14
	v_add_u32_e32 v41, v41, v59
	v_and_b32_e32 v16, 0x1ffffff, v16
	v_lshrrev_b32_e32 v54, 25, v18
	v_mul_u32_u24_e32 v55, 0xa8, v18
	v_lshrrev_b32_e32 v55, 20, v55
	v_min_u32_e32 v55, 31, v55
	v_xor_b32_e32 v55, s8, v55
	v_lshl_or_b32 v54, v54, 5, v55
	v_lshlrev_b32_e32 v56, 2, v54
	ds_read_b32 v56, v56
	v_lshrrev_b32_e32 v54, 25, v20
	v_mul_u32_u24_e32 v55, 0xa8, v20
	v_lshrrev_b32_e32 v55, 20, v55
	v_min_u32_e32 v55, 31, v55
	v_xor_b32_e32 v55, s8, v55
	v_lshl_or_b32 v54, v54, 5, v55
	v_lshlrev_b32_e32 v57, 2, v54
	ds_read_b32 v57, v57
	v_lshrrev_b32_e32 v54, 25, v22
	v_mul_u32_u24_e32 v55, 0xa8, v22
	v_lshrrev_b32_e32 v55, 20, v55
	v_min_u32_e32 v55, 31, v55
	v_xor_b32_e32 v55, s8, v55
	v_lshl_or_b32 v54, v54, 5, v55
	v_lshlrev_b32_e32 v58, 2, v54
	ds_read_b32 v58, v58
	v_lshrrev_b32_e32 v54, 25, v24
	v_mul_u32_u24_e32 v55, 0xa8, v24
	v_lshrrev_b32_e32 v55, 20, v55
	v_min_u32_e32 v55, 31, v55
	v_xor_b32_e32 v55, s8, v55
	v_lshl_or_b32 v54, v54, 5, v55
	v_lshlrev_b32_e32 v59, 2, v54
	ds_read_b32 v59, v59
	s_waitcnt lgkmcnt(0)
	v_add_u32_e32 v42, v42, v56
	v_and_b32_e32 v18, 0x1ffffff, v18
	v_add_u32_e32 v43, v43, v57
	v_and_b32_e32 v20, 0x1ffffff, v20
	v_add_u32_e32 v44, v44, v58
	v_and_b32_e32 v22, 0x1ffffff, v22
	v_add_u32_e32 v45, v45, v59
	v_and_b32_e32 v24, 0x1ffffff, v24
	v_lshrrev_b32_e32 v54, 25, v26
	v_mul_u32_u24_e32 v55, 0xa8, v26
	v_lshrrev_b32_e32 v55, 20, v55
	v_min_u32_e32 v55, 31, v55
	v_xor_b32_e32 v55, s8, v55
	v_lshl_or_b32 v54, v54, 5, v55
	v_lshlrev_b32_e32 v56, 2, v54
	ds_read_b32 v56, v56
	v_lshrrev_b32_e32 v54, 25, v28
	v_mul_u32_u24_e32 v55, 0xa8, v28
	v_lshrrev_b32_e32 v55, 20, v55
	v_min_u32_e32 v55, 31, v55
	v_xor_b32_e32 v55, s8, v55
	v_lshl_or_b32 v54, v54, 5, v55
	v_lshlrev_b32_e32 v57, 2, v54
	ds_read_b32 v57, v57
	v_lshrrev_b32_e32 v54, 25, v30
	v_mul_u32_u24_e32 v55, 0xa8, v30
	v_lshrrev_b32_e32 v55, 20, v55
	v_min_u32_e32 v55, 31, v55
	v_xor_b32_e32 v55, s8, v55
	v_lshl_or_b32 v54, v54, 5, v55
	v_lshlrev_b32_e32 v58, 2, v54
	ds_read_b32 v58, v58
	v_lshrrev_b32_e32 v54, 25, v32
	v_mul_u32_u24_e32 v55, 0xa8, v32
	v_lshrrev_b32_e32 v55, 20, v55
	v_min_u32_e32 v55, 31, v55
	v_xor_b32_e32 v55, s8, v55
	v_lshl_or_b32 v54, v54, 5, v55
	v_lshlrev_b32_e32 v59, 2, v54
	ds_read_b32 v59, v59
	s_waitcnt lgkmcnt(0)
	v_add_u32_e32 v46, v46, v56
	v_and_b32_e32 v26, 0x1ffffff, v26
	v_add_u32_e32 v47, v47, v57
	v_and_b32_e32 v28, 0x1ffffff, v28
	v_add_u32_e32 v48, v48, v58
	v_and_b32_e32 v30, 0x1ffffff, v30
	v_add_u32_e32 v49, v49, v59
	v_and_b32_e32 v32, 0x1ffffff, v32
	s_movk_i32 s14, 8000
	v_add_u32_e32 v54, 0, v0
	v_lshl_add_u32 v54, v54, 1, 0
	v_cmp_gt_i32_e32 vcc, s33, v54
	v_mov_b32_e32 v56, v34
	v_cmp_gt_u32_e64 s[4:5], s14, v56
	s_and_b64 vcc, vcc, s[4:5]
	v_lshlrev_b32_e32 v56, 3, v56
	s_and_saveexec_b64 s[4:5], vcc
	ds_write_b64 v56, v[2:3] offset:16448
	s_or_b64 exec, exec, s[4:5]
	v_add_u32_e32 v54, 0, v0
	v_lshl_add_u32 v54, v54, 1, 1
	v_cmp_gt_i32_e32 vcc, s33, v54
	v_mov_b32_e32 v56, v35
	v_cmp_gt_u32_e64 s[4:5], s14, v56
	s_and_b64 vcc, vcc, s[4:5]
	v_lshlrev_b32_e32 v56, 3, v56
	s_and_saveexec_b64 s[4:5], vcc
	ds_write_b64 v56, v[4:5] offset:16448
	s_or_b64 exec, exec, s[4:5]
	v_add_u32_e32 v54, 1024, v0
	v_lshl_add_u32 v54, v54, 1, 0
	v_cmp_gt_i32_e32 vcc, s33, v54
	v_mov_b32_e32 v56, v36
	v_cmp_gt_u32_e64 s[4:5], s14, v56
	s_and_b64 vcc, vcc, s[4:5]
	v_lshlrev_b32_e32 v56, 3, v56
	s_and_saveexec_b64 s[4:5], vcc
	ds_write_b64 v56, v[6:7] offset:16448
	s_or_b64 exec, exec, s[4:5]
	v_add_u32_e32 v54, 1024, v0
	v_lshl_add_u32 v54, v54, 1, 1
	v_cmp_gt_i32_e32 vcc, s33, v54
	v_mov_b32_e32 v56, v37
	v_cmp_gt_u32_e64 s[4:5], s14, v56
	s_and_b64 vcc, vcc, s[4:5]
	v_lshlrev_b32_e32 v56, 3, v56
	s_and_saveexec_b64 s[4:5], vcc
	ds_write_b64 v56, v[8:9] offset:16448
	s_or_b64 exec, exec, s[4:5]
	v_add_u32_e32 v54, 2048, v0
	v_lshl_add_u32 v54, v54, 1, 0
	v_cmp_gt_i32_e32 vcc, s33, v54
	v_mov_b32_e32 v56, v38
	v_cmp_gt_u32_e64 s[4:5], s14, v56
	s_and_b64 vcc, vcc, s[4:5]
	v_lshlrev_b32_e32 v56, 3, v56
	s_and_saveexec_b64 s[4:5], vcc
	ds_write_b64 v56, v[10:11] offset:16448
	s_or_b64 exec, exec, s[4:5]
	v_add_u32_e32 v54, 2048, v0
	v_lshl_add_u32 v54, v54, 1, 1
	v_cmp_gt_i32_e32 vcc, s33, v54
	v_mov_b32_e32 v56, v39
	v_cmp_gt_u32_e64 s[4:5], s14, v56
	s_and_b64 vcc, vcc, s[4:5]
	v_lshlrev_b32_e32 v56, 3, v56
	s_and_saveexec_b64 s[4:5], vcc
	ds_write_b64 v56, v[12:13] offset:16448
	s_or_b64 exec, exec, s[4:5]
	v_add_u32_e32 v54, 3072, v0
	v_lshl_add_u32 v54, v54, 1, 0
	v_cmp_gt_i32_e32 vcc, s33, v54
	v_mov_b32_e32 v56, v40
	v_cmp_gt_u32_e64 s[4:5], s14, v56
	s_and_b64 vcc, vcc, s[4:5]
	v_lshlrev_b32_e32 v56, 3, v56
	s_and_saveexec_b64 s[4:5], vcc
	ds_write_b64 v56, v[14:15] offset:16448
	s_or_b64 exec, exec, s[4:5]
	v_add_u32_e32 v54, 3072, v0
	v_lshl_add_u32 v54, v54, 1, 1
	v_cmp_gt_i32_e32 vcc, s33, v54
	v_mov_b32_e32 v56, v41
	v_cmp_gt_u32_e64 s[4:5], s14, v56
	s_and_b64 vcc, vcc, s[4:5]
	v_lshlrev_b32_e32 v56, 3, v56
	s_and_saveexec_b64 s[4:5], vcc
	ds_write_b64 v56, v[16:17] offset:16448
	s_or_b64 exec, exec, s[4:5]
	v_add_u32_e32 v54, 4096, v0
	v_lshl_add_u32 v54, v54, 1, 0
	v_cmp_gt_i32_e32 vcc, s33, v54
	v_mov_b32_e32 v56, v42
	v_cmp_gt_u32_e64 s[4:5], s14, v56
	s_and_b64 vcc, vcc, s[4:5]
	v_lshlrev_b32_e32 v56, 3, v56
	s_and_saveexec_b64 s[4:5], vcc
	ds_write_b64 v56, v[18:19] offset:16448
	s_or_b64 exec, exec, s[4:5]
	v_add_u32_e32 v54, 4096, v0
	v_lshl_add_u32 v54, v54, 1, 1
	v_cmp_gt_i32_e32 vcc, s33, v54
	v_mov_b32_e32 v56, v43
	v_cmp_gt_u32_e64 s[4:5], s14, v56
	s_and_b64 vcc, vcc, s[4:5]
	v_lshlrev_b32_e32 v56, 3, v56
	s_and_saveexec_b64 s[4:5], vcc
	ds_write_b64 v56, v[20:21] offset:16448
	s_or_b64 exec, exec, s[4:5]
	v_add_u32_e32 v54, 5120, v0
	v_lshl_add_u32 v54, v54, 1, 0
	v_cmp_gt_i32_e32 vcc, s33, v54
	v_mov_b32_e32 v56, v44
	v_cmp_gt_u32_e64 s[4:5], s14, v56
	s_and_b64 vcc, vcc, s[4:5]
	v_lshlrev_b32_e32 v56, 3, v56
	s_and_saveexec_b64 s[4:5], vcc
	ds_write_b64 v56, v[22:23] offset:16448
	s_or_b64 exec, exec, s[4:5]
	v_add_u32_e32 v54, 5120, v0
	v_lshl_add_u32 v54, v54, 1, 1
	v_cmp_gt_i32_e32 vcc, s33, v54
	v_mov_b32_e32 v56, v45
	v_cmp_gt_u32_e64 s[4:5], s14, v56
	s_and_b64 vcc, vcc, s[4:5]
	v_lshlrev_b32_e32 v56, 3, v56
	s_and_saveexec_b64 s[4:5], vcc
	ds_write_b64 v56, v[24:25] offset:16448
	s_or_b64 exec, exec, s[4:5]
	v_add_u32_e32 v54, 6144, v0
	v_lshl_add_u32 v54, v54, 1, 0
	v_cmp_gt_i32_e32 vcc, s33, v54
	v_mov_b32_e32 v56, v46
	v_cmp_gt_u32_e64 s[4:5], s14, v56
	s_and_b64 vcc, vcc, s[4:5]
	v_lshlrev_b32_e32 v56, 3, v56
	s_and_saveexec_b64 s[4:5], vcc
	ds_write_b64 v56, v[26:27] offset:16448
	s_or_b64 exec, exec, s[4:5]
	v_add_u32_e32 v54, 6144, v0
	v_lshl_add_u32 v54, v54, 1, 1
	v_cmp_gt_i32_e32 vcc, s33, v54
	v_mov_b32_e32 v56, v47
	v_cmp_gt_u32_e64 s[4:5], s14, v56
	s_and_b64 vcc, vcc, s[4:5]
	v_lshlrev_b32_e32 v56, 3, v56
	s_and_saveexec_b64 s[4:5], vcc
	ds_write_b64 v56, v[28:29] offset:16448
	s_or_b64 exec, exec, s[4:5]
	v_add_u32_e32 v54, 7168, v0
	v_lshl_add_u32 v54, v54, 1, 0
	v_cmp_gt_i32_e32 vcc, s33, v54
	v_mov_b32_e32 v56, v48
	v_cmp_gt_u32_e64 s[4:5], s14, v56
	s_and_b64 vcc, vcc, s[4:5]
	v_lshlrev_b32_e32 v56, 3, v56
	s_and_saveexec_b64 s[4:5], vcc
	ds_write_b64 v56, v[30:31] offset:16448
	s_or_b64 exec, exec, s[4:5]
	v_add_u32_e32 v54, 7168, v0
	v_lshl_add_u32 v54, v54, 1, 1
	v_cmp_gt_i32_e32 vcc, s33, v54
	v_mov_b32_e32 v56, v49
	v_cmp_gt_u32_e64 s[4:5], s14, v56
	s_and_b64 vcc, vcc, s[4:5]
	v_lshlrev_b32_e32 v56, 3, v56
	s_and_saveexec_b64 s[4:5], vcc
	ds_write_b64 v56, v[32:33] offset:16448
	s_or_b64 exec, exec, s[4:5]
	s_waitcnt lgkmcnt(0)
	s_barrier
	s_sub_i32 s6, s33, 0
	s_min_i32 s6, s6, 8000
	v_lshlrev_b32_e32 v59, 1, v0
	v_cmp_gt_i32_e32 vcc, s6, v59
	s_and_saveexec_b64 s[10:11], vcc
	s_cbranch_execz .Ll2_cpdone0
	v_add_u32_e32 v56, s36, v59
	v_ashrrev_i32_e32 v57, 31, v56
	v_lshl_add_u64 v[56:57], v[56:57], 3, s[40:41]
	v_lshlrev_b32_e32 v58, 4, v0
	s_mov_b64 s[4:5], 0
	s_mov_b64 s[12:13], 0x4000
